# v105 + chain prologue: first wait counts only the decay load (vmcnt 8) so the decay arithmetic overlaps tile 0's flight; k3/k6 exchange polls without s_sleep
# baseline (speedup 1.0000x reference)
.LBB0_697:
	s_lshl_b32 s10, s10, 5
	s_sub_i32 s13, 6, s74
	s_add_i32 s26, s74, 1
	v_lshrrev_b32_e32 v19, 1, v17
	s_and_b64 s[14:15], s[36:37], exec
	v_and_b32_e32 v32, 24, v19
	s_cselect_b32 s13, s26, s13
	v_and_b32_e32 v18, 15, v17
	v_lshlrev_b32_e32 v19, 1, v32
	v_lshlrev_b32_e32 v34, 2, v17
	s_add_i32 s13, s13, s12
	s_waitcnt vmcnt(8)
	v_mul_f32_e32 v17, 0xbfb8aa3b, v16
	v_lshl_or_b32 v210, s9, 6, v18
	v_lshl_or_b32 v33, v18, 6, v19
	s_lshl_b32 s12, s13, 9
	v_rndne_f32_e32 v18, v17
	s_mov_b32 s13, 0xbfb8aa3b
	v_sub_f32_e32 v19, v17, v18
	v_fma_f32 v17, v16, s13, -v17
	v_fmac_f32_e32 v17, 0xb2a5705f, v16
	v_add_f32_e32 v17, v19, v17
	v_exp_f32_e32 v17, v17
	v_cvt_i32_f32_e32 v18, v18
	s_or_b32 s48, s12, s11
	s_mov_b32 s11, 0x42ce8ed0
	s_and_b32 s10, s10, 0x60
	v_ldexp_f32 v17, v17, v18
	v_cmp_nlt_f32_e32 vcc, s11, v16
	s_mov_b32 s11, 0xc2b17218
	s_add_i32 m0, s7, 0x18000
	v_lshl_add_u64 v[8:9], v[8:9], 0, s[82:83]
	s_lshl_b32 s9, s9, 13
	s_lshl_b32 s14, s10, 7
	v_cndmask_b32_e32 v17, 0, v17, vcc
	v_cmp_ngt_f32_e32 vcc, s11, v16
	s_waitcnt vmcnt(2)
	s_barrier
	global_load_lds_dwordx4 v[8:9], off
	v_lshl_add_u64 v[6:7], v[6:7], 0, s[82:83]
	s_add_i32 m0, s7, 0x1a000
	s_add_i32 s87, s7, 0x8000
	s_add_i32 s88, s7, 0xa000
	v_cndmask_b32_e32 v35, v252, v17, vcc
	global_load_lds_dwordx4 v[6:7], off
	v_lshl_add_u64 v[2:3], v[2:3], 0, s[60:61]
	s_mov_b32 m0, s87
	s_add_u32 s12, s54, 0x20800
	v_add_f32_e32 v18, 1.0, v35
	global_load_lds_dwordx4 v[2:3], off
	v_lshl_add_u64 v[2:3], v[4:5], 0, s[60:61]
	s_mov_b32 m0, s88
	s_addc_u32 s13, s55, 0
	v_add_f32_e32 v16, -1.0, v18
	global_load_lds_dwordx4 v[2:3], off
	s_add_i32 m0, s7, 0x1c000
	v_lshl_add_u64 v[2:3], s[12:13], 0, v[200:201]
	v_sub_f32_e32 v17, v16, v18
	global_load_lds_dwordx4 v[2:3], off
	v_lshl_add_u64 v[2:3], s[12:13], 0, v[208:209]
	s_add_i32 m0, s7, 0x1e000
	v_add_f32_e32 v17, 1.0, v17
	v_sub_f32_e32 v16, v35, v16
	global_load_lds_dwordx4 v[2:3], off
	v_add_f32_e32 v19, v16, v17
	v_frexp_mant_f32_e32 v20, v18
	v_cvt_f64_f32_e32 v[16:17], v18
	s_mov_b32 s11, 0x3f2aaaab
	v_frexp_exp_i32_f64_e32 v16, v[16:17]
	v_cmp_gt_f32_e32 vcc, s11, v20
	s_mov_b32 s11, 0x3f317218
	v_lshlrev_b32_e32 v3, 14, v10
	v_subbrev_co_u32_e32 v24, vcc, 0, v16, vcc
	v_sub_u32_e32 v16, 0, v24
	v_ldexp_f32 v17, v18, v16
	v_add_f32_e32 v18, -1.0, v17
	v_add_f32_e32 v20, 1.0, v17
	v_ldexp_f32 v16, v19, v16
	v_add_f32_e32 v19, 1.0, v18
	v_add_f32_e32 v21, -1.0, v20
	v_sub_f32_e32 v19, v17, v19
	v_sub_f32_e32 v17, v17, v21
	v_add_f32_e32 v19, v16, v19
	v_add_f32_e32 v16, v16, v17
	v_add_f32_e32 v25, v20, v16
	v_rcp_f32_e32 v27, v25
	v_sub_f32_e32 v17, v20, v25
	v_add_f32_e32 v26, v16, v17
	v_add_f32_e32 v17, v18, v19
	v_mul_f32_e32 v29, v17, v27
	v_sub_f32_e32 v16, v18, v17
	v_mul_f32_e32 v18, v25, v29
	v_fma_f32 v20, v29, v25, -v18
	v_fmac_f32_e32 v20, v29, v26
	v_add_f32_e32 v28, v19, v16
	v_add_f32_e32 v16, v18, v20
	v_sub_f32_e32 v19, v17, v16
	v_pk_add_f32 v[22:23], v[16:17], v[18:19] neg_lo:[0,1] neg_hi:[0,1]
	v_mov_b32_e32 v21, v16
	v_pk_add_f32 v[16:17], v[22:23], v[20:21] neg_lo:[0,1] neg_hi:[0,1]
	v_and_b32_e32 v3, 0xffff8000, v3
	v_add_f32_e32 v17, v28, v17
	v_add_f32_e32 v16, v16, v17
	v_add_f32_e32 v17, v19, v16
	v_mul_f32_e32 v28, v27, v17
	v_mul_f32_e32 v18, v25, v28
	v_fma_f32 v20, v28, v25, -v18
	v_fmac_f32_e32 v20, v28, v26
	v_sub_f32_e32 v19, v19, v17
	v_add_f32_e32 v25, v16, v19
	v_add_f32_e32 v16, v18, v20
	v_sub_f32_e32 v19, v17, v16
	v_pk_add_f32 v[22:23], v[16:17], v[18:19] neg_lo:[0,1] neg_hi:[0,1]
	v_mov_b32_e32 v21, v16
	v_pk_add_f32 v[16:17], v[22:23], v[20:21] neg_lo:[0,1] neg_hi:[0,1]
	v_lshl_add_u32 v3, v11, 11, v3
	v_add_f32_e32 v17, v25, v17
	v_add_f32_e32 v16, v16, v17
	v_add_f32_e32 v17, v29, v28
	v_add_f32_e32 v16, v19, v16
	v_sub_f32_e32 v18, v17, v29
	v_mul_f32_e32 v16, v27, v16
	v_sub_f32_e32 v18, v28, v18
	v_add_f32_e32 v18, v18, v16
	v_add_f32_e32 v20, v17, v18
	v_mul_f32_e32 v21, v20, v20
	v_fmamk_f32 v16, v21, 0x3e9b6dac, v248
	v_fmaak_f32 v205, v21, v16, 0x3f2aaada
	v_cvt_f32_i32_e32 v16, v24
	v_sub_f32_e32 v17, v20, v17
	v_sub_f32_e32 v17, v18, v17
	v_ldexp_f32 v22, v17, 1
	v_mul_f32_e32 v17, v20, v21
	v_ldexp_f32 v19, v20, 1
	v_pk_mul_f32 v[20:21], v[16:17], v[204:205]
	v_and_b32_e32 v4, 1, v10
	v_fma_f32 v18, v16, s11, -v20
	v_fmac_f32_e32 v18, 0xb102e308, v16
	v_pk_add_f32 v[16:17], v[20:21], v[18:19]
	s_mov_b32 s11, 0x7f800000
	v_sub_f32_e32 v19, v17, v19
	v_sub_f32_e32 v19, v21, v19
	v_add_f32_e32 v23, v22, v19
	v_mov_b32_e32 v22, v20
	v_pk_add_f32 v[20:21], v[16:17], v[20:21] neg_lo:[0,1] neg_hi:[0,1]
	v_pk_add_f32 v[24:25], v[16:17], v[22:23]
	v_mov_b32_e32 v19, v16
	v_mov_b32_e32 v21, v25
	v_pk_add_f32 v[26:27], v[18:19], v[20:21] neg_lo:[0,1] neg_hi:[0,1]
	v_pk_add_f32 v[18:19], v[18:19], v[20:21]
	v_mov_b32_e32 v30, v17
	v_pk_add_f32 v[20:21], v[18:19], v[16:17] op_sel:[1,0] op_sel_hi:[0,1] neg_lo:[0,1] neg_hi:[0,1]
	v_pk_add_f32 v[28:29], v[24:25], v[20:21] op_sel_hi:[1,0] neg_lo:[0,1] neg_hi:[0,1]
	v_mov_b32_e32 v24, v25
	v_mov_b32_e32 v25, v19
	v_mov_b32_e32 v31, v20
	v_pk_add_f32 v[20:21], v[24:25], v[30:31] neg_lo:[0,1] neg_hi:[0,1]
	v_mov_b32_e32 v22, v23
	v_mov_b32_e32 v23, v16
	v_pk_add_f32 v[16:17], v[22:23], v[20:21] neg_lo:[0,1] neg_hi:[0,1]
	v_mov_b32_e32 v28, v26
	v_pk_add_f32 v[20:21], v[28:29], v[16:17]
	v_mov_b32_e32 v27, v19
	v_pk_add_f32 v[22:23], v[20:21], v[20:21] op_sel:[0,1] op_sel_hi:[1,0]
	v_cmp_neq_f32_e32 vcc, s11, v35
	v_pk_add_f32 v[18:19], v[18:19], v[22:23] op_sel:[1,0] op_sel_hi:[0,1]
	v_mov_b32_e32 v21, v18
	v_pk_add_f32 v[24:25], v[20:21], v[26:27] neg_lo:[0,1] neg_hi:[0,1]
	v_mov_b32_e32 v17, v22
	v_sub_f32_e32 v19, v20, v24
	v_pk_add_f32 v[16:17], v[16:17], v[24:25] neg_lo:[0,1] neg_hi:[0,1]
	v_sub_f32_e32 v19, v26, v19
	v_add_f32_e32 v16, v16, v19
	v_add_f32_e32 v16, v16, v17
	v_add_f32_e32 v16, v18, v16
	s_mov_b32 s11, 0x33800000
	v_cndmask_b32_e32 v16, v252, v16, vcc
	v_cmp_lt_f32_e64 vcc, |v35|, s11
	v_lshl_or_b32 v3, v4, 6, v3
	v_lshl_add_u32 v232, v12, 1, v3
	v_cndmask_b32_e32 v16, v16, v35, vcc
	v_mul_f32_e32 v2, 0xbfb8aa3b, v16
	v_mul_f32_e32 v2, 0x44000000, v2
	v_lshlrev_b32_e32 v3, 14, v13
	v_exp_f32_e32 v212, v2
	v_and_b32_e32 v3, 0xffff8000, v3
	v_and_b32_e32 v2, 32, v34
	v_lshl_add_u32 v3, v14, 11, v3
	v_and_b32_e32 v4, 1, v13
	v_bitop3_b32 v205, v33, s14, v2 bitop3:0xde
	v_bitop3_b32 v2, v33, s9, v2 bitop3:0xde
	s_waitcnt vmcnt(6)
	v_lshl_or_b32 v3, v4, 6, v3
	v_mov_b32_e32 v66, v67
	v_mov_b32_e32 v68, v67
	v_mov_b32_e32 v69, v67
	s_cmpk_lt_u32 s8, 0x100
	v_or_b32_e32 v216, s10, v32
	v_or_b32_e32 v218, 16, v210
	v_or_b32_e32 v220, 32, v210
	v_or_b32_e32 v222, 48, v210
	v_add_u32_e32 v224, 0x80, v210
	v_add_u32_e32 v226, 0x90, v210
	v_add_u32_e32 v228, 0xa0, v210
	v_add_u32_e32 v230, 0xb0, v210
	v_lshl_add_u32 v234, v15, 1, v3
	v_add_u32_e32 v217, 0, v2
	v_mov_b64_e32 v[2:3], v[66:67]
	v_mov_b64_e32 v[6:7], v[66:67]
	v_mov_b64_e32 v[10:11], v[66:67]
	v_mov_b64_e32 v[14:15], v[66:67]
	v_mov_b64_e32 v[18:19], v[66:67]
	v_mov_b64_e32 v[22:23], v[66:67]
	v_mov_b64_e32 v[26:27], v[66:67]
	v_mov_b64_e32 v[30:31], v[66:67]
	v_mov_b64_e32 v[34:35], v[66:67]
	v_mov_b64_e32 v[38:39], v[66:67]
	v_mov_b64_e32 v[42:43], v[66:67]
	v_mov_b64_e32 v[46:47], v[66:67]
	v_mov_b64_e32 v[50:51], v[66:67]
	v_mov_b64_e32 v[54:55], v[66:67]
	v_mov_b64_e32 v[58:59], v[66:67]
	v_mov_b64_e32 v[62:63], v[66:67]
	v_mov_b64_e32 v[72:73], v[68:69]
	v_mov_b64_e32 v[76:77], v[68:69]
	v_mov_b64_e32 v[80:81], v[68:69]
	v_mov_b64_e32 v[84:85], v[68:69]
	v_mov_b64_e32 v[88:89], v[68:69]
	v_mov_b64_e32 v[92:93], v[68:69]
	v_mov_b64_e32 v[96:97], v[68:69]
	v_mov_b64_e32 v[100:101], v[68:69]
	v_mov_b64_e32 v[104:105], v[68:69]
	v_mov_b64_e32 v[108:109], v[68:69]
	v_mov_b64_e32 v[112:113], v[68:69]
	v_mov_b64_e32 v[116:117], v[68:69]
	v_mov_b64_e32 v[120:121], v[68:69]
	v_mov_b64_e32 v[124:125], v[68:69]
	v_mov_b64_e32 v[128:129], v[68:69]
	v_mov_b64_e32 v[132:133], v[68:69]
	v_mov_b32_e32 v214, v212
	v_mov_b32_e32 v215, v212
	s_cselect_b64 s[42:43], -1, 0
	v_ashrrev_i32_e32 v211, 31, v210
	v_ashrrev_i32_e32 v219, 31, v218
	v_ashrrev_i32_e32 v221, 31, v220
	v_ashrrev_i32_e32 v223, 31, v222
	v_ashrrev_i32_e32 v225, 31, v224
	v_ashrrev_i32_e32 v227, 31, v226
	v_ashrrev_i32_e32 v229, 31, v228
	v_ashrrev_i32_e32 v231, 31, v230
	v_mov_b32_e32 v233, v67
	v_mov_b32_e32 v235, v67
	s_mov_b64 s[36:37], 0
	v_mov_b64_e32 v[4:5], v[68:69]
	v_mov_b64_e32 v[8:9], v[68:69]
	v_mov_b64_e32 v[12:13], v[68:69]
	v_mov_b64_e32 v[16:17], v[68:69]
	v_mov_b64_e32 v[20:21], v[68:69]
	v_mov_b64_e32 v[24:25], v[68:69]
	v_mov_b64_e32 v[28:29], v[68:69]
	v_mov_b64_e32 v[32:33], v[68:69]
	v_mov_b64_e32 v[36:37], v[68:69]
	v_mov_b64_e32 v[40:41], v[68:69]
	v_mov_b64_e32 v[44:45], v[68:69]
	v_mov_b64_e32 v[48:49], v[68:69]
	v_mov_b64_e32 v[52:53], v[68:69]
	v_mov_b64_e32 v[56:57], v[68:69]
	v_mov_b64_e32 v[60:61], v[68:69]
	v_mov_b64_e32 v[64:65], v[68:69]
	v_mov_b64_e32 v[70:71], v[66:67]
	v_mov_b64_e32 v[74:75], v[66:67]
	v_mov_b64_e32 v[78:79], v[66:67]
	v_mov_b64_e32 v[82:83], v[66:67]
	v_mov_b64_e32 v[86:87], v[66:67]
	v_mov_b64_e32 v[90:91], v[66:67]
	v_mov_b64_e32 v[94:95], v[66:67]
	v_mov_b64_e32 v[98:99], v[66:67]
	v_mov_b64_e32 v[102:103], v[66:67]
	v_mov_b64_e32 v[106:107], v[66:67]
	v_mov_b64_e32 v[110:111], v[66:67]
	v_mov_b64_e32 v[114:115], v[66:67]
	v_mov_b64_e32 v[118:119], v[66:67]
	v_mov_b64_e32 v[122:123], v[66:67]
	v_mov_b64_e32 v[126:127], v[66:67]
	v_mov_b64_e32 v[130:131], v[66:67]
	s_barrier
	s_branch .LBB0_700

.LBB0_834:
	v_mov_b64_e32 v[134:135], s[64:65]
	s_waitcnt vmcnt(0)
	flat_load_dword v134, v[134:135] sc1
	s_waitcnt vmcnt(0) lgkmcnt(0)
	v_readfirstlane_b32 s8, v134
	s_cmp_gt_u32 s8, 7
	s_cbranch_scc1 .LBB0_832
	s_memrealtime s[8:9]
	s_mov_b64 s[68:69], -1
	s_mov_b64 s[70:71], -1
	s_waitcnt lgkmcnt(0)
	s_sub_u32 s8, s8, s26
	s_subb_u32 s9, s9, s27
	v_cmp_lt_u64_e32 vcc, s[8:9], v[206:207]
	s_cbranch_vccz .LBB0_833
	s_nop 0
	s_mov_b64 s[70:71], 0
	s_branch .LBB0_833

.LBB0_1025:
	v_mov_b64_e32 v[60:61], s[34:35]
	flat_load_dword v60, v[60:61] sc1
	s_waitcnt vmcnt(0) lgkmcnt(0)
	v_readfirstlane_b32 s8, v60
	s_cmp_gt_u32 s8, 31
	s_cbranch_scc1 .LBB0_1023
	s_memrealtime s[8:9]
	s_mov_b64 s[70:71], -1
	s_mov_b64 s[74:75], -1
	s_waitcnt lgkmcnt(0)
	s_sub_u32 s8, s8, s26
	s_subb_u32 s9, s9, s27
	v_cmp_lt_u64_e32 vcc, s[8:9], v[206:207]
	s_cbranch_vccz .LBB0_1024
	s_nop 0
	s_mov_b64 s[74:75], 0
	s_branch .LBB0_1024
